# v29 + P6 streamer tail: carry kept in v40-43 (no per-iteration v_mov) and x64 scale via 4 v_pk_mul_f32 (loading-wave VALU per iteration roughly halved)
# baseline (speedup 1.0000x reference)
.LBB0_923:
	s_add_i32 s3, s94, 0x180
	s_add_i32 s4, s36, 0x180
	s_waitcnt lgkmcnt(0)
	s_barrier
	s_setprio 1
	v_mfma_scale_f32_16x16x128_f8f6f4 v[124:127], v[24:31], v[56:63], 0, v213, v213 op_sel_hi:[0,0,0]
	v_mfma_scale_f32_16x16x128_f8f6f4 v[120:123], v[16:23], v[56:63], 0, v213, v213 op_sel_hi:[0,0,0]
	v_mfma_scale_f32_16x16x128_f8f6f4 v[116:119], v[24:31], v[48:55], 0, v213, v213 op_sel_hi:[0,0,0]
	v_mfma_scale_f32_16x16x128_f8f6f4 v[112:115], v[16:23], v[48:55], 0, v213, v213 op_sel_hi:[0,0,0]
	v_mfma_scale_f32_16x16x128_f8f6f4 v[108:111], v[24:31], v[40:47], 0, v213, v213 op_sel_hi:[0,0,0]
	v_mfma_scale_f32_16x16x128_f8f6f4 v[104:107], v[16:23], v[40:47], 0, v213, v213 op_sel_hi:[0,0,0]
	v_mfma_scale_f32_16x16x128_f8f6f4 v[100:103], v[24:31], v[32:39], 0, v213, v213 op_sel_hi:[0,0,0]
	v_mfma_scale_f32_16x16x128_f8f6f4 v[96:99], v[16:23], v[32:39], 0, v213, v213 op_sel_hi:[0,0,0]
	s_setprio 0
	s_setprio 1
	v_mfma_scale_f32_16x16x128_f8f6f4 v[92:95], v[8:15], v[56:63], 0, v213, v213 op_sel_hi:[0,0,0]
	v_mfma_scale_f32_16x16x128_f8f6f4 v[88:91], v[0:7], v[56:63], 0, v213, v213 op_sel_hi:[0,0,0]
	v_mfma_scale_f32_16x16x128_f8f6f4 v[84:87], v[8:15], v[48:55], 0, v213, v213 op_sel_hi:[0,0,0]
	v_mfma_scale_f32_16x16x128_f8f6f4 v[80:83], v[0:7], v[48:55], 0, v213, v213 op_sel_hi:[0,0,0]
	v_mfma_scale_f32_16x16x128_f8f6f4 v[76:79], v[8:15], v[40:47], 0, v213, v213 op_sel_hi:[0,0,0]
	v_mfma_scale_f32_16x16x128_f8f6f4 v[72:75], v[0:7], v[40:47], 0, v213, v213 op_sel_hi:[0,0,0]
	v_mfma_scale_f32_16x16x128_f8f6f4 v[68:71], v[8:15], v[32:39], 0, v213, v213 op_sel_hi:[0,0,0]
	v_mfma_scale_f32_16x16x128_f8f6f4 v[64:67], v[0:7], v[32:39], 0, v213, v213 op_sel_hi:[0,0,0]
	s_setprio 0
	s_barrier
	ds_read_b128 v[24:27], v217 offset:0x8000
	ds_read_b128 v[28:31], v217 offset:0x8400
	ds_read_b128 v[16:19], v217 offset:0x8800
	ds_read_b128 v[20:23], v217 offset:0x8c00
	ds_read_b128 v[32:35], v216 offset:0x8000
	ds_read_b128 v[36:39], v216 offset:0x8400
	ds_read_b128 v[40:43], v216 offset:0x8800
	ds_read_b128 v[44:47], v216 offset:0x8c00
	ds_read_b128 v[48:51], v216 offset:0x9000
	ds_read_b128 v[52:55], v216 offset:0x9400
	ds_read_b128 v[56:59], v216 offset:0x9800
	ds_read_b128 v[60:63], v216 offset:0x9c00
	ds_read_b128 v[8:11], v217 offset:0xc000
	ds_read_b128 v[12:15], v217 offset:0xc400
	ds_read_b128 v[0:3], v217 offset:0xc800
	ds_read_b128 v[4:7], v217 offset:0xcc00
	s_mov_b32 m0, s76
	s_add_i32 s5, s94, 0x80100
	buffer_load_dwordx4 v214, s[12:15], s5 offen lds
	s_add_i32 s5, s94, 0xc0100
	s_mov_b32 m0, s77
	s_nop 0
	buffer_load_dwordx4 v214, s[12:15], s5 offen lds
	s_waitcnt vmcnt(10)
	s_waitcnt lgkmcnt(0)
	s_barrier
	s_setprio 1
	v_mfma_scale_f32_16x16x128_f8f6f4 v[188:191], v[24:31], v[32:39], v[188:191], v213, v213 op_sel_hi:[0,0,0]
	v_mfma_scale_f32_16x16x128_f8f6f4 v[184:187], v[16:23], v[32:39], v[184:187], v213, v213 op_sel_hi:[0,0,0]
	v_mfma_scale_f32_16x16x128_f8f6f4 v[180:183], v[24:31], v[40:47], v[180:183], v213, v213 op_sel_hi:[0,0,0]
	v_mfma_scale_f32_16x16x128_f8f6f4 v[176:179], v[16:23], v[40:47], v[176:179], v213, v213 op_sel_hi:[0,0,0]
	v_mfma_scale_f32_16x16x128_f8f6f4 v[172:175], v[24:31], v[48:55], v[172:175], v213, v213 op_sel_hi:[0,0,0]
	v_mfma_scale_f32_16x16x128_f8f6f4 v[168:171], v[16:23], v[48:55], v[168:171], v213, v213 op_sel_hi:[0,0,0]
	v_mfma_scale_f32_16x16x128_f8f6f4 v[164:167], v[24:31], v[56:63], v[164:167], v213, v213 op_sel_hi:[0,0,0]
	v_mfma_scale_f32_16x16x128_f8f6f4 v[160:163], v[16:23], v[56:63], v[160:163], v213, v213 op_sel_hi:[0,0,0]
	s_setprio 0
	s_setprio 1
	v_mfma_scale_f32_16x16x128_f8f6f4 v[156:159], v[8:15], v[32:39], v[156:159], v213, v213 op_sel_hi:[0,0,0]
	v_mfma_scale_f32_16x16x128_f8f6f4 v[152:155], v[0:7], v[32:39], v[152:155], v213, v213 op_sel_hi:[0,0,0]
	v_mfma_scale_f32_16x16x128_f8f6f4 v[148:151], v[8:15], v[40:47], v[148:151], v213, v213 op_sel_hi:[0,0,0]
	v_mfma_scale_f32_16x16x128_f8f6f4 v[144:147], v[0:7], v[40:47], v[144:147], v213, v213 op_sel_hi:[0,0,0]
	v_mfma_scale_f32_16x16x128_f8f6f4 v[140:143], v[8:15], v[48:55], v[140:143], v213, v213 op_sel_hi:[0,0,0]
	v_mfma_scale_f32_16x16x128_f8f6f4 v[136:139], v[0:7], v[48:55], v[136:139], v213, v213 op_sel_hi:[0,0,0]
	v_mfma_scale_f32_16x16x128_f8f6f4 v[132:135], v[8:15], v[56:63], v[132:135], v213, v213 op_sel_hi:[0,0,0]
	v_mfma_scale_f32_16x16x128_f8f6f4 v[128:131], v[0:7], v[56:63], v[128:131], v213, v213 op_sel_hi:[0,0,0]
	s_setprio 0
	s_barrier
	ds_read_b128 v[32:35], v216 offset:0xc000
	ds_read_b128 v[36:39], v216 offset:0xc400
	ds_read_b128 v[40:43], v216 offset:0xc800
	ds_read_b128 v[44:47], v216 offset:0xcc00
	ds_read_b128 v[48:51], v216 offset:0xd000
	ds_read_b128 v[52:55], v216 offset:0xd400
	ds_read_b128 v[56:59], v216 offset:0xd800
	ds_read_b128 v[60:63], v216 offset:0xdc00
	s_mov_b32 m0, s80
	s_mov_b32 s10, s14
	s_mov_b32 s11, s15
	buffer_load_dwordx4 v215, s[8:11], s4 offen lds
	s_add_i32 s4, s36, 0x80180
	s_mov_b32 m0, s81
	s_nop 0
	buffer_load_dwordx4 v215, s[8:11], s4 offen lds
	s_add_i32 s4, s36, 0x8180
	s_mov_b32 m0, s84
	s_nop 0
	buffer_load_dwordx4 v215, s[8:11], s4 offen lds
	s_add_i32 s4, s36, 0x88180
	s_mov_b32 m0, s85
	s_nop 0
	buffer_load_dwordx4 v215, s[8:11], s4 offen lds
	s_mov_b32 m0, s82
	s_nop 0
	buffer_load_dwordx4 v214, s[12:15], s3 offen lds
	s_add_i32 s3, s94, 0x40180
	s_mov_b32 m0, s83
	s_nop 0
	buffer_load_dwordx4 v214, s[12:15], s3 offen lds
	s_waitcnt vmcnt(8)
	s_waitcnt lgkmcnt(0)
	s_barrier
	s_setprio 1
	v_mfma_scale_f32_16x16x128_f8f6f4 v[124:127], v[24:31], v[32:39], v[124:127], v213, v213 op_sel_hi:[0,0,0]
	v_mfma_scale_f32_16x16x128_f8f6f4 v[120:123], v[16:23], v[32:39], v[120:123], v213, v213 op_sel_hi:[0,0,0]
	v_mfma_scale_f32_16x16x128_f8f6f4 v[116:119], v[24:31], v[40:47], v[116:119], v213, v213 op_sel_hi:[0,0,0]
	v_mfma_scale_f32_16x16x128_f8f6f4 v[112:115], v[16:23], v[40:47], v[112:115], v213, v213 op_sel_hi:[0,0,0]
	v_mfma_scale_f32_16x16x128_f8f6f4 v[108:111], v[24:31], v[48:55], v[108:111], v213, v213 op_sel_hi:[0,0,0]
	v_mfma_scale_f32_16x16x128_f8f6f4 v[104:107], v[16:23], v[48:55], v[104:107], v213, v213 op_sel_hi:[0,0,0]
	v_mfma_scale_f32_16x16x128_f8f6f4 v[100:103], v[24:31], v[56:63], v[100:103], v213, v213 op_sel_hi:[0,0,0]
	v_mfma_scale_f32_16x16x128_f8f6f4 v[96:99], v[16:23], v[56:63], v[96:99], v213, v213 op_sel_hi:[0,0,0]
	s_setprio 0
	s_setprio 1
	v_mfma_scale_f32_16x16x128_f8f6f4 v[92:95], v[8:15], v[32:39], v[92:95], v213, v213 op_sel_hi:[0,0,0]
	v_mfma_scale_f32_16x16x128_f8f6f4 v[88:91], v[0:7], v[32:39], v[88:91], v213, v213 op_sel_hi:[0,0,0]
	v_mfma_scale_f32_16x16x128_f8f6f4 v[84:87], v[8:15], v[40:47], v[84:87], v213, v213 op_sel_hi:[0,0,0]
	v_mfma_scale_f32_16x16x128_f8f6f4 v[80:83], v[0:7], v[40:47], v[80:83], v213, v213 op_sel_hi:[0,0,0]
	v_mfma_scale_f32_16x16x128_f8f6f4 v[76:79], v[8:15], v[48:55], v[76:79], v213, v213 op_sel_hi:[0,0,0]
	v_mfma_scale_f32_16x16x128_f8f6f4 v[72:75], v[0:7], v[48:55], v[72:75], v213, v213 op_sel_hi:[0,0,0]
	v_mfma_scale_f32_16x16x128_f8f6f4 v[68:71], v[8:15], v[56:63], v[68:71], v213, v213 op_sel_hi:[0,0,0]
	v_mfma_scale_f32_16x16x128_f8f6f4 v[64:67], v[0:7], v[56:63], v[64:67], v213, v213 op_sel_hi:[0,0,0]
	s_setprio 0
	s_barrier
	s_waitcnt vmcnt(14)
	v_mul_f32_e32 v0, 0x42800000, v196
	v_mul_f32_e32 v1, 0x42800000, v192
	v_mul_f32_e32 v2, 0x42800000, v197
	v_mul_f32_e32 v3, 0x42800000, v193
	v_mul_f32_e32 v4, 0x42800000, v198
	v_mul_f32_e32 v5, 0x42800000, v194
	v_mul_f32_e32 v6, 0x42800000, v199
	v_mul_f32_e32 v7, 0x42800000, v195
	v_cvt_pk_fp8_f32 v202, v1, v0
	v_cvt_pk_fp8_f32 v219, v3, v2
	v_cvt_pk_fp8_f32 v220, v5, v4
	v_cvt_pk_fp8_f32 v221, v7, v6
	s_add_i32 s61, s36, 0x200
	s_mov_b32 s33, 0
	s_mov_b32 s79, s66
	s_mov_b32 s90, s68
	s_branch .LBB0_926
.LBB0_926:
	v_mov_b32_e32 v40, v202
	v_mov_b32_e32 v41, v219
	v_mov_b32_e32 v42, v220
	v_mov_b32_e32 v43, v221
.Lp6_top:
	s_add_i32 s4, s94, s33
	s_mov_b32 s64, s90
	s_add_i32 s90, s90, 1
	s_add_i32 s3, s4, 0x200
	s_add_i32 s5, s61, s33
	ds_read_b128 v[24:27], v217 offset:0
	ds_read_b128 v[28:31], v217 offset:0x400
	ds_read_b128 v[16:19], v217 offset:0x800
	ds_read_b128 v[20:23], v217 offset:0xc00
	ds_read_b128 v[46:49], v216 offset:0
	ds_read_b128 v[50:53], v216 offset:0x400
	ds_read_b128 v[54:57], v216 offset:0x800
	ds_read_b128 v[58:61], v216 offset:0xc00
	ds_read_b128 v[192:195], v216 offset:0x1000
	ds_read_b128 v[196:199], v216 offset:0x1400
	ds_read_b128 v[220:223], v216 offset:0x1800
	ds_read_b128 v[224:227], v216 offset:0x1c00
	ds_read_b128 v[8:11], v217 offset:0x4000
	ds_read_b128 v[12:15], v217 offset:0x4400
	ds_read_b128 v[0:3], v217 offset:0x4800
	ds_read_b128 v[4:7], v217 offset:0x4c00
	s_cmpk_eq_i32 s33, 0xe00
	s_cselect_b32 s65, s60, s3
	s_cselect_b32 s16, s95, s5
	s_add_i32 s3, s65, 0x80
	s_mov_b32 m0, s86
	s_add_i32 s5, s4, 0x80180
	buffer_load_dwordx4 v214, s[12:15], s5 offen lds
	s_add_i32 s4, s4, 0xc0180
	s_mov_b32 m0, s89
	s_add_i32 s17, s16, 0x80
	buffer_load_dwordx4 v214, s[12:15], s4 offen lds
	s_lshr_b32 s4, s90, 2
	s_mul_i32 s5, s4, s34
	s_add_i32 s36, s5, s2
	s_cmp_lt_i32 s4, s47
	s_cselect_b64 s[4:5], -1, 0
	s_and_b64 s[62:63], s[4:5], exec
	s_cselect_b32 s67, s36, 0
	s_ashr_i32 s62, s67, 7
	s_bfe_u32 s36, s90, 0x10001
	s_ashr_i32 s63, s62, 31
	s_or_b32 s78, s36, s87
	s_bfe_u32 s36, s67, 0x20005
	s_lshl_b64 vcc, s[62:63], 23
	s_add_u32 vcc_lo, s28, vcc_lo
	s_addc_u32 vcc_hi, s29, vcc_hi
	s_lshl_b32 s38, s36, 21
	s_add_u32 s38, vcc_lo, s38
	s_addc_u32 s39, vcc_hi, 0
	s_lshl_b32 s67, s67, 7
	s_and_b32 s67, s67, 0xf80
	s_lshl_b32 vcc_lo, s67, 2
	s_add_u32 vcc_lo, s38, vcc_lo
	v_and_or_b32 v202, s79, 2, v200
	s_addc_u32 vcc_hi, s39, 0
	v_lshl_or_b32 v44, s78, 5, v218
	v_lshlrev_b64 v[32:33], 14, v[202:203]
	v_lshl_add_u64 v[32:33], vcc, 0, v[32:33]
	v_lshlrev_b32_e32 v202, 2, v44
	v_lshl_add_u64 v[32:33], v[32:33], 0, v[202:203]
	s_movk_i32 s38, 0x4000
	v_add_co_u32_e32 v36, vcc, s38, v32
	s_nop 1
	v_addc_co_u32_e32 v37, vcc, 0, v33, vcc
	global_load_dwordx4 v[32:35], v[32:33], off nt
	s_nop 0
	global_load_dwordx4 v[36:39], v[36:37], off nt
	s_waitcnt vmcnt(10)
	s_waitcnt lgkmcnt(0)
	s_barrier
	s_setprio 1
	v_mfma_scale_f32_16x16x128_f8f6f4 v[188:191], v[24:31], v[46:53], v[188:191], v213, v213 op_sel_hi:[0,0,0]
	v_mfma_scale_f32_16x16x128_f8f6f4 v[184:187], v[16:23], v[46:53], v[184:187], v213, v213 op_sel_hi:[0,0,0]
	v_mfma_scale_f32_16x16x128_f8f6f4 v[180:183], v[24:31], v[54:61], v[180:183], v213, v213 op_sel_hi:[0,0,0]
	v_mfma_scale_f32_16x16x128_f8f6f4 v[176:179], v[16:23], v[54:61], v[176:179], v213, v213 op_sel_hi:[0,0,0]
	v_mfma_scale_f32_16x16x128_f8f6f4 v[172:175], v[24:31], v[192:199], v[172:175], v213, v213 op_sel_hi:[0,0,0]
	v_mfma_scale_f32_16x16x128_f8f6f4 v[168:171], v[16:23], v[192:199], v[168:171], v213, v213 op_sel_hi:[0,0,0]
	v_mfma_scale_f32_16x16x128_f8f6f4 v[164:167], v[24:31], v[220:227], v[164:167], v213, v213 op_sel_hi:[0,0,0]
	v_mfma_scale_f32_16x16x128_f8f6f4 v[160:163], v[16:23], v[220:227], v[160:163], v213, v213 op_sel_hi:[0,0,0]
	s_setprio 0
	s_setprio 1
	v_mfma_scale_f32_16x16x128_f8f6f4 v[156:159], v[8:15], v[46:53], v[156:159], v213, v213 op_sel_hi:[0,0,0]
	v_mfma_scale_f32_16x16x128_f8f6f4 v[152:155], v[0:7], v[46:53], v[152:155], v213, v213 op_sel_hi:[0,0,0]
	v_mfma_scale_f32_16x16x128_f8f6f4 v[148:151], v[8:15], v[54:61], v[148:151], v213, v213 op_sel_hi:[0,0,0]
	v_mfma_scale_f32_16x16x128_f8f6f4 v[144:147], v[0:7], v[54:61], v[144:147], v213, v213 op_sel_hi:[0,0,0]
	v_mfma_scale_f32_16x16x128_f8f6f4 v[140:143], v[8:15], v[192:199], v[140:143], v213, v213 op_sel_hi:[0,0,0]
	v_mfma_scale_f32_16x16x128_f8f6f4 v[136:139], v[0:7], v[192:199], v[136:139], v213, v213 op_sel_hi:[0,0,0]
	v_mfma_scale_f32_16x16x128_f8f6f4 v[132:135], v[8:15], v[220:227], v[132:135], v213, v213 op_sel_hi:[0,0,0]
	v_mfma_scale_f32_16x16x128_f8f6f4 v[128:131], v[0:7], v[220:227], v[128:131], v213, v213 op_sel_hi:[0,0,0]
	s_setprio 0
	s_barrier
	ds_read_b128 v[46:49], v216 offset:0x4000
	ds_read_b128 v[50:53], v216 offset:0x4400
	ds_read_b128 v[54:57], v216 offset:0x4800
	ds_read_b128 v[58:61], v216 offset:0x4c00
	ds_read_b128 v[192:195], v216 offset:0x5000
	ds_read_b128 v[196:199], v216 offset:0x5400
	ds_read_b128 v[220:223], v216 offset:0x5800
	ds_read_b128 v[224:227], v216 offset:0x5c00
	s_mov_b32 m0, s71
	s_nop 0
	buffer_load_dwordx4 v215, s[8:11], s16 offen lds
	s_add_i32 s38, s16, 0x80000
	s_mov_b32 m0, s72
	s_nop 0
	buffer_load_dwordx4 v215, s[8:11], s38 offen lds
	s_add_i32 s38, s16, 0x8000
	s_mov_b32 m0, s73
	s_nop 0
	buffer_load_dwordx4 v215, s[8:11], s38 offen lds
	s_add_i32 s38, s16, 0x88000
	s_mov_b32 m0, s74
	s_nop 0
	buffer_load_dwordx4 v215, s[8:11], s38 offen lds
	s_mov_b32 m0, s70
	s_add_i32 s38, s65, 0x40000
	buffer_load_dwordx4 v214, s[12:15], s65 offen lds
	s_mov_b32 m0, s75
	s_nop 0
	buffer_load_dwordx4 v214, s[12:15], s38 offen lds
	s_waitcnt vmcnt(10)
	s_waitcnt lgkmcnt(0)
	s_barrier
	s_setprio 1
	v_mfma_scale_f32_16x16x128_f8f6f4 v[124:127], v[24:31], v[46:53], v[124:127], v213, v213 op_sel_hi:[0,0,0]
	v_mfma_scale_f32_16x16x128_f8f6f4 v[120:123], v[16:23], v[46:53], v[120:123], v213, v213 op_sel_hi:[0,0,0]
	v_mfma_scale_f32_16x16x128_f8f6f4 v[116:119], v[24:31], v[54:61], v[116:119], v213, v213 op_sel_hi:[0,0,0]
	v_mfma_scale_f32_16x16x128_f8f6f4 v[112:115], v[16:23], v[54:61], v[112:115], v213, v213 op_sel_hi:[0,0,0]
	v_mfma_scale_f32_16x16x128_f8f6f4 v[108:111], v[24:31], v[192:199], v[108:111], v213, v213 op_sel_hi:[0,0,0]
	v_mfma_scale_f32_16x16x128_f8f6f4 v[104:107], v[16:23], v[192:199], v[104:107], v213, v213 op_sel_hi:[0,0,0]
	v_mfma_scale_f32_16x16x128_f8f6f4 v[100:103], v[24:31], v[220:227], v[100:103], v213, v213 op_sel_hi:[0,0,0]
	v_mfma_scale_f32_16x16x128_f8f6f4 v[96:99], v[16:23], v[220:227], v[96:99], v213, v213 op_sel_hi:[0,0,0]
	s_setprio 0
	s_setprio 1
	v_mfma_scale_f32_16x16x128_f8f6f4 v[92:95], v[8:15], v[46:53], v[92:95], v213, v213 op_sel_hi:[0,0,0]
	v_mfma_scale_f32_16x16x128_f8f6f4 v[88:91], v[0:7], v[46:53], v[88:91], v213, v213 op_sel_hi:[0,0,0]
	v_mfma_scale_f32_16x16x128_f8f6f4 v[84:87], v[8:15], v[54:61], v[84:87], v213, v213 op_sel_hi:[0,0,0]
	v_mfma_scale_f32_16x16x128_f8f6f4 v[80:83], v[0:7], v[54:61], v[80:83], v213, v213 op_sel_hi:[0,0,0]
	v_mfma_scale_f32_16x16x128_f8f6f4 v[76:79], v[8:15], v[192:199], v[76:79], v213, v213 op_sel_hi:[0,0,0]
	v_mfma_scale_f32_16x16x128_f8f6f4 v[72:75], v[0:7], v[192:199], v[72:75], v213, v213 op_sel_hi:[0,0,0]
	v_mfma_scale_f32_16x16x128_f8f6f4 v[68:71], v[8:15], v[220:227], v[68:71], v213, v213 op_sel_hi:[0,0,0]
	v_mfma_scale_f32_16x16x128_f8f6f4 v[64:67], v[0:7], v[220:227], v[64:67], v213, v213 op_sel_hi:[0,0,0]
	s_setprio 0
	s_barrier
	ds_read_b128 v[16:19], v217 offset:0x8000
	ds_read_b128 v[20:23], v217 offset:0x8400
	ds_read_b128 v[24:27], v217 offset:0x8800
	ds_read_b128 v[28:31], v217 offset:0x8c00
	ds_read_b128 v[46:49], v216 offset:0x8000
	ds_read_b128 v[50:53], v216 offset:0x8400
	ds_read_b128 v[54:57], v216 offset:0x8800
	ds_read_b128 v[58:61], v216 offset:0x8c00
	ds_read_b128 v[192:195], v216 offset:0x9000
	ds_read_b128 v[196:199], v216 offset:0x9400
	ds_read_b128 v[220:223], v216 offset:0x9800
	ds_read_b128 v[224:227], v216 offset:0x9c00
	ds_read_b128 v[8:11], v217 offset:0xc000
	ds_read_b128 v[12:15], v217 offset:0xc400
	ds_read_b128 v[0:3], v217 offset:0xc800
	ds_read_b128 v[4:7], v217 offset:0xcc00
	s_mov_b32 m0, s76
	s_add_i32 s38, s65, 0x80000
	buffer_load_dwordx4 v214, s[12:15], s38 offen lds
	s_add_i32 s38, s65, 0xc0000
	s_mov_b32 m0, s77
	s_nop 0
	buffer_load_dwordx4 v214, s[12:15], s38 offen lds
	s_waitcnt vmcnt(10)
	s_waitcnt lgkmcnt(0)
	s_barrier
	s_setprio 1
	v_mfma_scale_f32_16x16x128_f8f6f4 v[188:191], v[16:23], v[46:53], v[188:191], v213, v213 op_sel_hi:[0,0,0]
	v_mfma_scale_f32_16x16x128_f8f6f4 v[184:187], v[24:31], v[46:53], v[184:187], v213, v213 op_sel_hi:[0,0,0]
	v_mfma_scale_f32_16x16x128_f8f6f4 v[180:183], v[16:23], v[54:61], v[180:183], v213, v213 op_sel_hi:[0,0,0]
	v_mfma_scale_f32_16x16x128_f8f6f4 v[176:179], v[24:31], v[54:61], v[176:179], v213, v213 op_sel_hi:[0,0,0]
	v_mfma_scale_f32_16x16x128_f8f6f4 v[172:175], v[16:23], v[192:199], v[172:175], v213, v213 op_sel_hi:[0,0,0]
	v_mfma_scale_f32_16x16x128_f8f6f4 v[168:171], v[24:31], v[192:199], v[168:171], v213, v213 op_sel_hi:[0,0,0]
	v_mfma_scale_f32_16x16x128_f8f6f4 v[164:167], v[16:23], v[220:227], v[164:167], v213, v213 op_sel_hi:[0,0,0]
	v_mfma_scale_f32_16x16x128_f8f6f4 v[160:163], v[24:31], v[220:227], v[160:163], v213, v213 op_sel_hi:[0,0,0]
	s_setprio 0
	s_setprio 1
	v_mfma_scale_f32_16x16x128_f8f6f4 v[156:159], v[8:15], v[46:53], v[156:159], v213, v213 op_sel_hi:[0,0,0]
	v_mfma_scale_f32_16x16x128_f8f6f4 v[152:155], v[0:7], v[46:53], v[152:155], v213, v213 op_sel_hi:[0,0,0]
	v_mfma_scale_f32_16x16x128_f8f6f4 v[148:151], v[8:15], v[54:61], v[148:151], v213, v213 op_sel_hi:[0,0,0]
	v_mfma_scale_f32_16x16x128_f8f6f4 v[144:147], v[0:7], v[54:61], v[144:147], v213, v213 op_sel_hi:[0,0,0]
	v_mfma_scale_f32_16x16x128_f8f6f4 v[140:143], v[8:15], v[192:199], v[140:143], v213, v213 op_sel_hi:[0,0,0]
	v_mfma_scale_f32_16x16x128_f8f6f4 v[136:139], v[0:7], v[192:199], v[136:139], v213, v213 op_sel_hi:[0,0,0]
	v_mfma_scale_f32_16x16x128_f8f6f4 v[132:135], v[8:15], v[220:227], v[132:135], v213, v213 op_sel_hi:[0,0,0]
	v_mfma_scale_f32_16x16x128_f8f6f4 v[128:131], v[0:7], v[220:227], v[128:131], v213, v213 op_sel_hi:[0,0,0]
	s_setprio 0
	s_barrier
	ds_read_b128 v[46:49], v216 offset:0xc000
	ds_read_b128 v[50:53], v216 offset:0xc400
	ds_read_b128 v[54:57], v216 offset:0xc800
	ds_read_b128 v[58:61], v216 offset:0xcc00
	ds_read_b128 v[192:195], v216 offset:0xd000
	ds_read_b128 v[196:199], v216 offset:0xd400
	ds_read_b128 v[220:223], v216 offset:0xd800
	ds_read_b128 v[224:227], v216 offset:0xdc00
	s_mov_b32 m0, s80
	s_nop 0
	buffer_load_dwordx4 v215, s[8:11], s17 offen lds
	s_add_i32 s17, s16, 0x80080
	s_mov_b32 m0, s81
	s_add_i32 s65, s65, 0x40080
	buffer_load_dwordx4 v215, s[8:11], s17 offen lds
	s_add_i32 s17, s16, 0x8080
	s_mov_b32 m0, s84
	s_add_i32 s16, s16, 0x88080
	buffer_load_dwordx4 v215, s[8:11], s17 offen lds
	s_mov_b32 m0, s85
	s_nop 0
	buffer_load_dwordx4 v215, s[8:11], s16 offen lds
	s_mov_b32 m0, s82
	s_nop 0
	buffer_load_dwordx4 v214, s[12:15], s3 offen lds
	s_mov_b32 m0, s83
	s_nop 0
	buffer_load_dwordx4 v214, s[12:15], s65 offen lds
	s_waitcnt vmcnt(8)
	s_waitcnt lgkmcnt(0)
	s_barrier
	s_setprio 1
	v_mfma_scale_f32_16x16x128_f8f6f4 v[124:127], v[16:23], v[46:53], v[124:127], v213, v213 op_sel_hi:[0,0,0]
	v_mfma_scale_f32_16x16x128_f8f6f4 v[120:123], v[24:31], v[46:53], v[120:123], v213, v213 op_sel_hi:[0,0,0]
	v_mfma_scale_f32_16x16x128_f8f6f4 v[116:119], v[16:23], v[54:61], v[116:119], v213, v213 op_sel_hi:[0,0,0]
	v_mfma_scale_f32_16x16x128_f8f6f4 v[112:115], v[24:31], v[54:61], v[112:115], v213, v213 op_sel_hi:[0,0,0]
	v_mfma_scale_f32_16x16x128_f8f6f4 v[108:111], v[16:23], v[192:199], v[108:111], v213, v213 op_sel_hi:[0,0,0]
	v_mfma_scale_f32_16x16x128_f8f6f4 v[104:107], v[24:31], v[192:199], v[104:107], v213, v213 op_sel_hi:[0,0,0]
	v_mfma_scale_f32_16x16x128_f8f6f4 v[100:103], v[16:23], v[220:227], v[100:103], v213, v213 op_sel_hi:[0,0,0]
	v_mfma_scale_f32_16x16x128_f8f6f4 v[96:99], v[24:31], v[220:227], v[96:99], v213, v213 op_sel_hi:[0,0,0]
	s_setprio 0
	s_setprio 1
	v_mfma_scale_f32_16x16x128_f8f6f4 v[92:95], v[8:15], v[46:53], v[92:95], v213, v213 op_sel_hi:[0,0,0]
	v_mfma_scale_f32_16x16x128_f8f6f4 v[88:91], v[0:7], v[46:53], v[88:91], v213, v213 op_sel_hi:[0,0,0]
	v_mfma_scale_f32_16x16x128_f8f6f4 v[84:87], v[8:15], v[54:61], v[84:87], v213, v213 op_sel_hi:[0,0,0]
	v_mfma_scale_f32_16x16x128_f8f6f4 v[80:83], v[0:7], v[54:61], v[80:83], v213, v213 op_sel_hi:[0,0,0]
	v_mfma_scale_f32_16x16x128_f8f6f4 v[76:79], v[8:15], v[192:199], v[76:79], v213, v213 op_sel_hi:[0,0,0]
	v_mfma_scale_f32_16x16x128_f8f6f4 v[72:75], v[0:7], v[192:199], v[72:75], v213, v213 op_sel_hi:[0,0,0]
	v_mfma_scale_f32_16x16x128_f8f6f4 v[68:71], v[8:15], v[220:227], v[68:71], v213, v213 op_sel_hi:[0,0,0]
	v_mfma_scale_f32_16x16x128_f8f6f4 v[64:67], v[0:7], v[220:227], v[64:67], v213, v213 op_sel_hi:[0,0,0]
	s_setprio 0
	s_barrier
	s_bitcmp0_b32 s64, 0
	s_waitcnt vmcnt(14)
	s_mov_b32 s100, 0x42800000
	s_mov_b32 s101, 0x42800000
	v_pk_mul_f32 v[0:1], v[32:33], s[100:101]
	v_pk_mul_f32 v[2:3], v[34:35], s[100:101]
	v_pk_mul_f32 v[4:5], v[36:37], s[100:101]
	v_pk_mul_f32 v[6:7], v[38:39], s[100:101]
	s_mov_b64 s[64:65], -1
	s_cbranch_scc0 .LBB0_929
	s_andn2_b64 vcc, exec, s[64:65]
	s_cbranch_vccnz .LBB0_925
	s_branch .LBB0_930
